# baseline (speedup 1.0000x reference)
.LBB0_20:
	v_mov_b32_e32 v81, 0
	v_lshlrev_b32_e32 v4, 3, v0
	v_lshrrev_b32_e32 v2, 2, v0
	v_lshlrev_b32_e32 v3, 1, v0
	v_bfe_i32 v5, v0, 0, 1
	v_lshrrev_b32_e32 v0, 5, v0
	v_and_b32_e32 v5, 0x120, v5
	v_and_b32_e32 v221, 12, v0
	v_add_u16_e32 v0, v214, v212
	v_add_u32_e32 v5, v50, v5
	v_mul_u32_u24_e32 v1, 0x2800, v1
	v_lshrrev_b16_e32 v0, 1, v0
	v_or_b32_e32 v1, v1, v214
	v_lshl_add_u32 v223, v0, 2, v5
	v_add_lshl_u32 v0, v214, v212, 1
	v_lshlrev_b32_e32 v216, 2, v51
	s_movk_i32 s0, 0x88
	v_add_u32_e32 v222, 0x22a00, v1
	v_add_u32_e32 v1, 64, v0
	v_add_u32_e32 v0, 0xc0, v0
	v_and_or_b32 v2, v2, 3, v216
	v_lshlrev_b32_e32 v6, 4, v212
	v_mad_u32_u24 v8, v212, s0, v50
	v_and_b32_e32 v0, 0x1fc, v0
	s_movk_i32 s0, 0x880
	v_mul_u32_u24_e32 v2, 0x88, v2
	v_and_b32_e32 v3, 32, v3
	v_add_u32_e32 v7, v50, v6
	v_add_u32_e32 v225, v5, v0
	v_mad_u32_u24 v0, v51, s0, v50
	s_movk_i32 s0, 0x240
	v_and_b32_e32 v4, 24, v4
	v_add3_u32 v2, v50, v2, v3
	v_and_b32_e32 v1, 0xfc, v1
	v_add3_u32 v226, v0, v6, s0
	v_add_u32_e32 v228, v7, v214
	v_mbcnt_lo_u32_b32 v0, -1, 0
	v_and_b32_e32 v80, 0xffff, v39
	v_mov_b32_e32 v82, v81
	v_mov_b32_e32 v83, v81
	v_and_b32_e32 v204, 0xffff, v38
	v_mov_b32_e32 v205, v81
	v_mov_b32_e32 v206, v81
	v_mov_b32_e32 v207, v81
	v_lshl_add_u32 v220, v215, 1, v50
	v_add_u32_e32 v224, v5, v1
	s_brev_b32 s33, 61
	s_brev_b32 s34, 60
	s_mov_b32 s35, 0x7fff7fff
	s_mov_b32 s42, 0xa714a714
	v_mov_b32_e32 v227, 0xb7d0b7d0
	s_mov_b32 s43, 0xbc90bc90
	v_add_u32_e32 v229, v8, v214
	v_add_u32_e32 v230, v2, v4
	v_add_u32_e32 v231, 0xf0, v228
	v_add_u32_e32 v232, 0x170, v228
	v_add_u32_e32 v233, 0x1f0, v228
	v_add_u32_e32 v234, 0x70, v228
	v_mbcnt_hi_u32_b32 v235, -1, v0
	v_add_u32_e32 v246, 0x2000, v229
	v_xor_b32_e32 v245, 32, v235
	v_lshlrev_b32_e32 v245, 2, v245
	v_and_b32_e32 v247, 15, v215
	v_lshrrev_b32_e32 v248, 4, v215
	s_movk_i32 s0, 0x2440
	v_and_b32_e32 v249, 1, v215
	v_lshlrev_b32_e32 v249, 2, v249
	v_bfe_u32 v250, v215, 1, 1
	v_lshl_add_u32 v249, v250, 1, v249
	v_bfe_u32 v250, v215, 2, 1
	v_lshl_add_u32 v249, v250, 3, v249
	v_bfe_u32 v250, v215, 3, 1
	v_add_u32_e32 v249, v249, v250
	v_mul_u32_u24_e32 v249, 0x88, v249
	v_lshl_add_u32 v249, v248, 4, v249
	v_add3_u32 v249, v249, v50, s0
	v_add_u32_e32 v250, 0x880, v249
	v_bfe_u32 v251, v215, 3, 1
	v_lshlrev_b32_e32 v251, 4, v251
	v_bfe_u32 v252, v215, 5, 1
	v_add_u32_e32 v251, v251, v252
	v_bfe_u32 v252, v215, 4, 1
	v_lshl_add_u32 v251, v252, 3, v251
	v_bfe_u32 v252, v215, 2, 1
	v_lshl_add_u32 v251, v252, 2, v251
	v_mul_u32_u24_e32 v251, 0x88, v251
	v_and_b32_e32 v252, 3, v215
	v_lshl_add_u32 v251, v252, 3, v251
	v_add3_u32 v251, v251, v50, s0
	v_sub_u32_e32 v252, v222, v214
	v_lshl_add_u32 v252, v248, 3, v252
	v_lshlrev_b32_e32 v253, 7, v247
	v_lshl_add_u32 v253, v248, 4, v253
	s_movk_i32 s0, 0x3540
	v_add3_u32 v248, v253, v50, s0
	v_xor_b32_e32 v247, 16, v215
	v_lshlrev_b32_e32 v247, 2, v247
	s_waitcnt vmcnt(28)
	s_branch .LBB0_22

.LBB0_24:
	v_sub_f32_e32 v24, v32, v237
	v_exp_f32_e32 v24, v24
	v_sub_f32_e32 v25, v33, v237
	v_exp_f32_e32 v25, v25
	v_sub_f32_e32 v26, v34, v237
	v_exp_f32_e32 v26, v26
	v_sub_f32_e32 v27, v35, v237
	v_exp_f32_e32 v27, v27
	v_sub_f32_e32 v28, v36, v237
	v_exp_f32_e32 v28, v28
	v_sub_f32_e32 v29, v37, v237
	v_exp_f32_e32 v29, v29
	v_sub_f32_e32 v30, v38, v237
	v_exp_f32_e32 v30, v30
	v_sub_f32_e32 v31, v39, v237
	v_exp_f32_e32 v31, v31
	ds_read_b64_tr_b16 v[48:49], v251
	ds_read_b64_tr_b16 v[50:51], v251 offset:272
	ds_read_b64_tr_b16 v[52:53], v251 offset:32
	ds_read_b64_tr_b16 v[54:55], v251 offset:304
	ds_read_b64_tr_b16 v[56:57], v251 offset:64
	ds_read_b64_tr_b16 v[58:59], v251 offset:336
	ds_read_b64_tr_b16 v[60:61], v251 offset:96
	ds_read_b64_tr_b16 v[62:63], v251 offset:368
	v_cvt_pk_f16_f32 v40, v24, v25
	v_cvt_pk_f16_f32 v41, v28, v29
	v_cvt_pk_f16_f32 v42, v26, v27
	v_cvt_pk_f16_f32 v43, v30, v31
	v_dot2c_f32_f16_e32 v236, 0x3c003c00, v40
	v_dot2c_f32_f16_e32 v236, 0x3c003c00, v41
	v_dot2c_f32_f16_e32 v236, 0x3c003c00, v42
	v_dot2c_f32_f16_e32 v236, 0x3c003c00, v43
	s_waitcnt lgkmcnt(6)
	v_mfma_f32_16x16x32_f16 v[0:3], v[48:51], v[40:43], v[0:3]
	s_waitcnt lgkmcnt(4)
	v_mfma_f32_16x16x32_f16 v[4:7], v[52:55], v[40:43], v[4:7]
	s_addk_i32 s8, 0x200
	s_waitcnt lgkmcnt(2)
	v_mfma_f32_16x16x32_f16 v[8:11], v[56:59], v[40:43], v[8:11]
	s_cmpk_eq_i32 s8, 0x800
	s_waitcnt lgkmcnt(0)
	v_mfma_f32_16x16x32_f16 v[12:15], v[60:63], v[40:43], v[12:15]
	s_cbranch_scc1 .LBB0_28
